# speedup vs baseline: 1.0418x; 1.0009x over previous
.LBB0_4:
	s_or_b64 exec, exec, s[4:5]
	s_cmp_eq_u32 s94, 0
	s_cbranch_scc1 .LBB0_64
	s_add_i32 s85, s85, 1
	v_min_i32_e32 v21, s40, v20
	v_lshl_add_u32 v21, v21, 12, v17
	global_load_dwordx4 v[86:89], v21, s[38:39] sc0 sc1 nt
	v_add_u32_e32 v22, 4, v20
	v_min_i32_e32 v22, s40, v22
	v_lshl_add_u32 v22, v22, 12, v17
	global_load_dwordx4 v[74:77], v22, s[38:39] sc0 sc1 nt
	v_add_u32_e32 v21, 8, v20
	v_min_i32_e32 v21, s40, v21
	v_lshl_add_u32 v21, v21, 12, v17
	global_load_dwordx4 v[78:81], v21, s[38:39] sc0 sc1 nt
	v_add_u32_e32 v22, 12, v20
	v_min_i32_e32 v22, s40, v22
	v_lshl_add_u32 v22, v22, 12, v17
	global_load_dwordx4 v[58:61], v22, s[38:39] sc0 sc1 nt
	v_add_u32_e32 v21, 16, v20
	v_min_i32_e32 v21, s40, v21
	v_lshl_add_u32 v21, v21, 12, v17
	global_load_dwordx4 v[62:65], v21, s[38:39] sc0 sc1 nt
	v_add_u32_e32 v22, 20, v20
	v_min_i32_e32 v22, s40, v22
	v_lshl_add_u32 v22, v22, 12, v17
	global_load_dwordx4 v[50:53], v22, s[38:39] sc0 sc1 nt
	v_add_u32_e32 v21, 24, v20
	v_min_i32_e32 v21, s40, v21
	v_lshl_add_u32 v21, v21, 12, v17
	global_load_dwordx4 v[54:57], v21, s[38:39] sc0 sc1 nt
	v_add_u32_e32 v22, 28, v20
	v_min_i32_e32 v22, s40, v22
	v_lshl_add_u32 v22, v22, 12, v17
	global_load_dwordx4 v[178:181], v22, s[38:39] sc0 sc1 nt
	s_mov_b64 s[4:5], 0
	s_waitcnt lgkmcnt(0)
	s_barrier

.LBB0_7:
	s_add_i32 s95, s82, -1
	s_lshl_b32 s90, s91, 6
	s_add_i32 s96, s3, -1
	s_add_i32 s88, s89, s33
	s_cmp_lg_u32 s85, 0
	s_cbranch_scc1 .Litem_loaded
	v_mov_b32_e32 v2, v0
	s_add_i32 s95, s82, -1
	s_lshl_b32 s90, s91, 6
	v_ashrrev_i32_e32 v52, 4, v2
	v_bfe_u32 v53, v2, 4, 2
	v_lshlrev_b32_e32 v2, 2, v2
	s_cmp_gt_i32 s82, 1
	v_and_or_b32 v2, v2, 60, s90
	s_cselect_b32 s4, 64, 0
	s_add_i32 s96, s3, -1
	v_lshlrev_b64 v[4:5], 2, v[2:3]
	v_min_i32_e32 v2, s96, v52
	v_add_lshl_u32 v2, v2, s76, 10
	v_lshlrev_b64 v[8:9], 2, v[2:3]
	v_add_u32_e32 v2, 32, v52
	v_min_i32_e32 v2, s96, v2
	s_waitcnt lgkmcnt(0)
	v_lshl_add_u64 v[6:7], s[70:71], 0, v[4:5]
	v_add_lshl_u32 v2, v2, s76, 10
	v_lshl_add_u64 v[10:11], v[6:7], 0, v[8:9]
	v_lshlrev_b64 v[12:13], 2, v[2:3]
	v_lshl_add_u64 v[14:15], v[6:7], 0, v[12:13]
	global_load_dwordx4 v[70:73], v[10:11], off
	global_load_dwordx4 v[66:69], v[14:15], off
	v_lshl_add_u64 v[10:11], s[74:75], 0, v[4:5]
	v_lshl_add_u64 v[16:17], v[10:11], 0, v[8:9]
	v_lshl_add_u64 v[50:51], v[10:11], 0, v[12:13]
	global_load_dwordx4 v[182:185], v[16:17], off
	global_load_dwordx4 v[186:189], v[50:51], off
	v_add_u32_e32 v50, s4, v52
	v_min_i32_e32 v2, s96, v50
	v_add_lshl_u32 v2, v2, s76, 10
	v_lshl_add_u64 v[16:17], v[2:3], 2, v[6:7]
	v_add_u32_e32 v2, 32, v50
	v_min_i32_e32 v2, s96, v2
	v_add_lshl_u32 v2, v2, s76, 10
	s_min_i32 s5, s95, 2
	v_lshl_add_u64 v[50:51], v[2:3], 2, v[6:7]
	global_load_dwordx4 v[90:93], v[16:17], off
	global_load_dwordx4 v[82:85], v[50:51], off
	v_lshl_add_u32 v50, s5, 6, v52
	v_min_i32_e32 v2, s96, v50
	v_add_lshl_u32 v2, v2, s76, 10
	v_lshl_add_u64 v[16:17], v[2:3], 2, v[6:7]
	v_add_u32_e32 v2, 32, v50
	v_min_i32_e32 v2, s96, v2
	s_add_i32 s88, s89, s33
	v_add_lshl_u32 v2, v2, s76, 10
	v_add_u32_e32 v54, s88, v53
	v_lshl_add_u64 v[6:7], v[2:3], 2, v[6:7]
	v_min_i32_e32 v2, s96, v54
	v_lshl_add_u64 v[4:5], s[68:69], 0, v[4:5]
	v_add_lshl_u32 v2, v2, s76, 10
	global_load_dwordx4 v[98:101], v[16:17], off
	global_load_dwordx4 v[94:97], v[6:7], off
	v_lshl_add_u64 v[6:7], v[2:3], 2, v[4:5]
	v_add_u32_e32 v2, 4, v54
	v_min_i32_e32 v2, s96, v2
	v_add_lshl_u32 v2, v2, s76, 10
	v_lshl_add_u64 v[16:17], v[2:3], 2, v[4:5]
	v_add_u32_e32 v2, 8, v54
	v_min_i32_e32 v2, s96, v2
	v_add_lshl_u32 v2, v2, s76, 10
	global_load_dwordx4 v[86:89], v[6:7], off sc0 sc1 nt
	global_load_dwordx4 v[74:77], v[16:17], off sc0 sc1 nt
	v_lshl_add_u64 v[6:7], v[2:3], 2, v[4:5]
	v_add_u32_e32 v2, 12, v54
	v_min_i32_e32 v2, s96, v2
	v_add_lshl_u32 v2, v2, s76, 10
	v_lshl_add_u64 v[16:17], v[2:3], 2, v[4:5]
	v_add_u32_e32 v2, 16, v54
	v_min_i32_e32 v2, s96, v2
	v_add_lshl_u32 v2, v2, s76, 10
	global_load_dwordx4 v[78:81], v[6:7], off sc0 sc1 nt
	global_load_dwordx4 v[58:61], v[16:17], off sc0 sc1 nt
	v_lshl_add_u64 v[6:7], v[2:3], 2, v[4:5]
	v_add_u32_e32 v2, 20, v54
	v_min_i32_e32 v2, s96, v2
	v_add_lshl_u32 v2, v2, s76, 10
	v_lshl_add_u64 v[16:17], v[2:3], 2, v[4:5]
	v_add_u32_e32 v2, 24, v54
	v_min_i32_e32 v2, s96, v2
	v_add_lshl_u32 v2, v2, s76, 10
	global_load_dwordx4 v[62:65], v[6:7], off sc0 sc1 nt
	global_load_dwordx4 v[50:53], v[16:17], off sc0 sc1 nt
	v_lshl_add_u64 v[16:17], v[2:3], 2, v[4:5]
	v_add_u32_e32 v2, 28, v54
	v_min_i32_e32 v2, s96, v2
	v_add_lshl_u32 v2, v2, s76, 10
	v_lshl_add_u64 v[102:103], v[2:3], 2, v[4:5]
	global_load_dwordx4 v[54:57], v[16:17], off sc0 sc1 nt
	global_load_dwordx4 v[178:181], v[102:103], off sc0 sc1 nt
